# in-proj tile selection: generic division by the group size (always 8) replaced by shift/mask; MoE-down epilogue: redundant zeroing of the fp8 pack destinations removed
# baseline (speedup 1.0000x reference)
;     __device__ bool next(int i, Unit& u) const {
;         const long L = (long)i * G + c; if (L >= nwg) return false;
;         int wgid = (int)L; { const int q = nwg / NXCD, r = nwg % NXCD, xcd = wgid % NXCD, off = wgid / NXCD; wgid = (xcd < r ? xcd * (q + 1) : r * (q + 1) + (xcd - r) * q) + off; }
;         const int nig = WGM * nN, gid = wgid / nig, fm = gid * WGM, gsz = (nM - fm) < WGM ? (nM - fm) : WGM;
;         u.pm = fm + ((wgid % nig) % gsz); u.pn = (wgid % nig) / gsz; u.e = 0; u.r0 = 0; return true;
.LBB0_188:
	s_add_i32 s30, s30, 1
	s_mul_i32 s2, s30, s41
	s_mul_hi_u32 s3, s30, s20
	s_add_i32 s3, s3, s2
	s_mul_i32 s2, s30, s20
	v_readlane_b32 s10, v245, 18
	s_add_u32 s10, s2, s10
	s_addc_u32 s11, s3, s19
	v_cmp_gt_i64_e64 s[2:3], s[10:11], v[168:169]
	s_and_b64 vcc, exec, s[2:3]
	s_cbranch_vccnz .LBB0_190
	s_ashr_i32 s33, s10, 31
	s_lshr_b32 s33, s33, 29
	s_add_i32 s33, s10, s33
	s_ashr_i32 s43, s33, 3
	s_and_b32 s33, s33, -8
	s_sub_i32 s33, s10, s33
	s_cmp_lt_i32 s33, 0
	s_cselect_b32 s44, s21, 0xe0
	s_mul_i32 s33, s33, s44
	s_add_i32 s33, s33, s43
	s_mul_hi_i32 s43, s33, 0x92492493
	s_add_i32 s43, s43, s33
	s_lshr_b32 s44, s43, 31
	s_ashr_i32 s43, s43, 7
	s_add_i32 s43, s43, s44
	s_lshl_b32 s44, s43, 3
	s_mulk_i32 s43, 0xe0
	s_sub_i32 s33, s33, s43
	s_lshr_b32 s43, s33, 3
	s_and_b32 s33, s33, 7
	s_add_i32 s44, s44, s33

; __device__ __forceinline__ unsigned cvt4_fp8(float a, float b, float c, float d) { int w = 0; w = __builtin_amdgcn_cvt_pk_fp8_f32(a, b, w, false); w = __builtin_amdgcn_cvt_pk_fp8_f32(c, d, w, true); return (unsigned)w; }
;     __device__ __forceinline__ void operator()(const f32x4 (&acc)[2][2][4][2], const pg8::Unit& u, const Pre& pre, int wr, int wc, int fr, int fq) const {
;         const int e = u.e, cn = u.pn - e * 8, col0 = cn * 256 + wc * 32 + 8 * fq;
;         f32x4 bv[2][2];
; #pragma unroll
;         for (int bj = 0; bj < 2; ++bj) { bv[bj][0] = pre.bv[bj][0]; bv[bj][1] = pre.bv[bj][1]; }
; #pragma unroll
;         for (int ai = 0; ai < 2; ++ai)
; #pragma unroll
;             for (int m = 0; m < 4; ++m) { unsigned char* rowp = YS + (size_t)(u.pm * 256 + ai * 128 + wr * 64 + m * 16 + fr) * DM + col0;
; #pragma unroll
;                 for (int bj = 0; bj < 2; ++bj) { const f32x4 v0 = acc[ai][bj][m][0] * 0.015625f + bv[bj][0], v1 = acc[ai][bj][m][1] * 0.015625f + bv[bj][1];
;                     u32x2 w; w.x = cvt4_fp8(v0[0], v0[1], v0[2], v0[3]); w.y = cvt4_fp8(v1[0], v1[1], v1[2], v1[3]);
;                     *(u32x2*)(rowp + bj * 128) = w; } }
.LBB0_1010:
	s_nop 15
	s_nop 3
	s_waitcnt vmcnt(18)
	v_pk_fma_f32 v[8:9], v[158:159], s[18:19], v[26:27] op_sel_hi:[1,0,1]
	v_pk_fma_f32 v[10:11], v[154:155], s[18:19], v[22:23] op_sel_hi:[1,0,1]
	v_cvt_pk_fp8_f32 v12, v8, v9
	v_cvt_pk_fp8_f32 v13, v10, v11
	v_mov_b32_e32 v3, v0
	v_pk_fma_f32 v[8:9], v[160:161], s[18:19], v[28:29] op_sel_hi:[1,0,1]
	v_readfirstlane_b32 s10, v3
	v_pk_fma_f32 v[10:11], v[156:157], s[18:19], v[24:25] op_sel_hi:[1,0,1]
	s_lshr_b32 s33, s10, 1
	s_ashr_i32 s10, s10, 2
	v_cvt_pk_fp8_f32 v12, v8, v9 op_sel:[0,0,1]
	v_cvt_pk_fp8_f32 v13, v10, v11 op_sel:[0,0,1]
	s_waitcnt vmcnt(16)
	v_pk_fma_f32 v[8:9], v[150:151], s[18:19], v[30:31] op_sel_hi:[1,0,1]
	v_pk_fma_f32 v[10:11], v[146:147], s[18:19], v[18:19] op_sel_hi:[1,0,1]
	s_andn2_b32 s10, s10, 63
	v_cvt_pk_fp8_f32 v14, v8, v9
	v_cvt_pk_fp8_f32 v15, v10, v11
	s_lshl_b32 s11, s65, 8
	s_lshl_b32 s65, s66, 11
	v_and_or_b32 v4, v3, 15, s10
	s_and_b32 s33, s33, 0x60
	s_sub_i32 s11, s11, s65
	v_lshl_add_u32 v4, s62, 8, v4
	v_lshrrev_b32_e32 v2, 1, v3
	s_or_b32 s11, s33, s11
	v_ashrrev_i32_e32 v5, 31, v4
	v_pk_fma_f32 v[8:9], v[152:153], s[18:19], v[32:33] op_sel_hi:[1,0,1]
	v_pk_fma_f32 v[10:11], v[148:149], s[18:19], v[20:21] op_sel_hi:[1,0,1]
	v_and_or_b32 v2, v2, 24, s11
	v_lshlrev_b64 v[6:7], 11, v[4:5]
	v_cvt_pk_fp8_f32 v14, v8, v9 op_sel:[0,0,1]
	v_cvt_pk_fp8_f32 v15, v10, v11 op_sel:[0,0,1]
	v_ashrrev_i32_e32 v3, 31, v2
	v_lshl_add_u64 v[6:7], s[14:15], 0, v[6:7]
	v_lshl_add_u64 v[6:7], v[6:7], 0, v[2:3]
	global_store_dwordx2 v[6:7], v[12:13], off
	global_store_dwordx2 v[6:7], v[14:15], off offset:128
	v_pk_fma_f32 v[8:9], v[142:143], s[18:19], v[26:27] op_sel_hi:[1,0,1]
	v_pk_fma_f32 v[10:11], v[138:139], s[18:19], v[22:23] op_sel_hi:[1,0,1]
	v_cvt_pk_fp8_f32 v12, v8, v9
	v_cvt_pk_fp8_f32 v13, v10, v11
	v_pk_fma_f32 v[8:9], v[144:145], s[18:19], v[28:29] op_sel_hi:[1,0,1]
	v_pk_fma_f32 v[10:11], v[140:141], s[18:19], v[24:25] op_sel_hi:[1,0,1]
	v_cvt_pk_fp8_f32 v12, v8, v9 op_sel:[0,0,1]
	v_cvt_pk_fp8_f32 v13, v10, v11 op_sel:[0,0,1]
	v_pk_fma_f32 v[8:9], v[134:135], s[18:19], v[30:31] op_sel_hi:[1,0,1]
	v_pk_fma_f32 v[10:11], v[130:131], s[18:19], v[18:19] op_sel_hi:[1,0,1]
	v_cvt_pk_fp8_f32 v14, v8, v9
	v_cvt_pk_fp8_f32 v15, v10, v11
	v_or_b32_e32 v6, 16, v4
	v_ashrrev_i32_e32 v7, 31, v6
	v_pk_fma_f32 v[8:9], v[136:137], s[18:19], v[32:33] op_sel_hi:[1,0,1]
	v_pk_fma_f32 v[10:11], v[132:133], s[18:19], v[20:21] op_sel_hi:[1,0,1]
	v_lshlrev_b64 v[6:7], 11, v[6:7]
	v_cvt_pk_fp8_f32 v14, v8, v9 op_sel:[0,0,1]
	v_cvt_pk_fp8_f32 v15, v10, v11 op_sel:[0,0,1]
	v_lshl_add_u64 v[6:7], s[14:15], 0, v[6:7]
	v_lshl_add_u64 v[6:7], v[6:7], 0, v[2:3]
	global_store_dwordx2 v[6:7], v[12:13], off
	global_store_dwordx2 v[6:7], v[14:15], off offset:128
	v_pk_fma_f32 v[8:9], v[126:127], s[18:19], v[26:27] op_sel_hi:[1,0,1]
	v_pk_fma_f32 v[10:11], v[122:123], s[18:19], v[22:23] op_sel_hi:[1,0,1]
	v_cvt_pk_fp8_f32 v12, v8, v9
	v_cvt_pk_fp8_f32 v13, v10, v11
	v_pk_fma_f32 v[8:9], v[128:129], s[18:19], v[28:29] op_sel_hi:[1,0,1]
	v_pk_fma_f32 v[10:11], v[124:125], s[18:19], v[24:25] op_sel_hi:[1,0,1]
	v_cvt_pk_fp8_f32 v12, v8, v9 op_sel:[0,0,1]
	v_cvt_pk_fp8_f32 v13, v10, v11 op_sel:[0,0,1]
	v_pk_fma_f32 v[8:9], v[118:119], s[18:19], v[30:31] op_sel_hi:[1,0,1]
	v_pk_fma_f32 v[10:11], v[114:115], s[18:19], v[18:19] op_sel_hi:[1,0,1]
	v_cvt_pk_fp8_f32 v14, v8, v9
	v_cvt_pk_fp8_f32 v15, v10, v11
	v_or_b32_e32 v6, 32, v4
	v_ashrrev_i32_e32 v7, 31, v6
	v_pk_fma_f32 v[8:9], v[120:121], s[18:19], v[32:33] op_sel_hi:[1,0,1]
	v_pk_fma_f32 v[10:11], v[116:117], s[18:19], v[20:21] op_sel_hi:[1,0,1]
	v_lshlrev_b64 v[6:7], 11, v[6:7]
	v_cvt_pk_fp8_f32 v14, v8, v9 op_sel:[0,0,1]
	v_cvt_pk_fp8_f32 v15, v10, v11 op_sel:[0,0,1]
	v_lshl_add_u64 v[6:7], s[14:15], 0, v[6:7]
	v_lshl_add_u64 v[6:7], v[6:7], 0, v[2:3]
	global_store_dwordx2 v[6:7], v[12:13], off
	global_store_dwordx2 v[6:7], v[14:15], off offset:128
	v_pk_fma_f32 v[8:9], v[110:111], s[18:19], v[26:27] op_sel_hi:[1,0,1]
	v_pk_fma_f32 v[10:11], v[106:107], s[18:19], v[22:23] op_sel_hi:[1,0,1]
	v_cvt_pk_fp8_f32 v12, v8, v9
	v_cvt_pk_fp8_f32 v13, v10, v11
	v_pk_fma_f32 v[8:9], v[112:113], s[18:19], v[28:29] op_sel_hi:[1,0,1]
	v_pk_fma_f32 v[10:11], v[108:109], s[18:19], v[24:25] op_sel_hi:[1,0,1]
	v_cvt_pk_fp8_f32 v12, v8, v9 op_sel:[0,0,1]
	v_cvt_pk_fp8_f32 v13, v10, v11 op_sel:[0,0,1]
	v_pk_fma_f32 v[8:9], v[102:103], s[18:19], v[30:31] op_sel_hi:[1,0,1]
	v_pk_fma_f32 v[10:11], v[98:99], s[18:19], v[18:19] op_sel_hi:[1,0,1]
	v_cvt_pk_fp8_f32 v14, v8, v9
	v_cvt_pk_fp8_f32 v15, v10, v11
	v_or_b32_e32 v6, 48, v4
	v_ashrrev_i32_e32 v7, 31, v6
	v_pk_fma_f32 v[8:9], v[104:105], s[18:19], v[32:33] op_sel_hi:[1,0,1]
	v_pk_fma_f32 v[10:11], v[100:101], s[18:19], v[20:21] op_sel_hi:[1,0,1]
	v_lshlrev_b64 v[6:7], 11, v[6:7]
	v_cvt_pk_fp8_f32 v14, v8, v9 op_sel:[0,0,1]
	v_cvt_pk_fp8_f32 v15, v10, v11 op_sel:[0,0,1]
; __device__ __forceinline__ unsigned cvt4_fp8(float a, float b, float c, float d) { int w = 0; w = __builtin_amdgcn_cvt_pk_fp8_f32(a, b, w, false); w = __builtin_amdgcn_cvt_pk_fp8_f32(c, d, w, true); return (unsigned)w; }
; #define PG8_BAR __builtin_amdgcn_s_barrier()
; template <class Epi, class Sched, bool GATHER, bool ALIGN_EPI, bool SP2, bool FP8>
; __device__ __forceinline__ void gemm_phase(LAS unsigned char* lds, const Gemm g, const Sched& S, const Epi& E) {
;     ...
;         if (!has_next) break;
; #pragma unroll
;         for (int a = 0; a < 2; ++a)
; #pragma unroll
;             for (int b = 0; b < 2; ++b)
; #pragma unroll
;                 for (int m = 0; m < 4; ++m)
; #pragma unroll
;                     for (int n = 0; n < 2; ++n) acc[a][b][m][n] = (f32x4){0.f, 0.f, 0.f, 0.f};
;         cur = nxt; cA = nA; cB = nB; ++ui;
;         vA0 = nvA0; vA1 = nvA1;
;         if constexpr (ALIGN_EPI) { if (wr == 1) PG8_BAR; }
;     __device__ __forceinline__ void operator()(const f32x4 (&acc)[2][2][4][2], const pg8::Unit& u, const Pre& pre, int wr, int wc, int fr, int fq) const {
;     ...
;         for (int ai = 0; ai < 2; ++ai)
; #pragma unroll
;             for (int m = 0; m < 4; ++m) { unsigned char* rowp = YS + (size_t)(u.pm * 256 + ai * 128 + wr * 64 + m * 16 + fr) * DM + col0;
; #pragma unroll
;                 for (int bj = 0; bj < 2; ++bj) { const f32x4 v0 = acc[ai][bj][m][0] * 0.015625f + bv[bj][0], v1 = acc[ai][bj][m][1] * 0.015625f + bv[bj][1];
;                     u32x2 w; w.x = cvt4_fp8(v0[0], v0[1], v0[2], v0[3]); w.y = cvt4_fp8(v1[0], v1[1], v1[2], v1[3]);
;                     *(u32x2*)(rowp + bj * 128) = w; } }
	v_lshl_add_u64 v[6:7], s[14:15], 0, v[6:7]
	v_lshl_add_u64 v[6:7], v[6:7], 0, v[2:3]
	global_store_dwordx2 v[6:7], v[12:13], off
	global_store_dwordx2 v[6:7], v[14:15], off offset:128
	v_pk_fma_f32 v[8:9], v[94:95], s[18:19], v[26:27] op_sel_hi:[1,0,1]
	v_pk_fma_f32 v[10:11], v[90:91], s[18:19], v[22:23] op_sel_hi:[1,0,1]
	v_cvt_pk_fp8_f32 v12, v8, v9
	v_cvt_pk_fp8_f32 v13, v10, v11
	v_pk_fma_f32 v[8:9], v[96:97], s[18:19], v[28:29] op_sel_hi:[1,0,1]
	v_pk_fma_f32 v[10:11], v[92:93], s[18:19], v[24:25] op_sel_hi:[1,0,1]
	v_cvt_pk_fp8_f32 v12, v8, v9 op_sel:[0,0,1]
	v_cvt_pk_fp8_f32 v13, v10, v11 op_sel:[0,0,1]
	v_pk_fma_f32 v[8:9], v[86:87], s[18:19], v[30:31] op_sel_hi:[1,0,1]
	v_pk_fma_f32 v[10:11], v[82:83], s[18:19], v[18:19] op_sel_hi:[1,0,1]
	v_cvt_pk_fp8_f32 v14, v8, v9
	v_cvt_pk_fp8_f32 v15, v10, v11
	v_add_u32_e32 v6, 0x80, v4
	v_ashrrev_i32_e32 v7, 31, v6
	v_pk_fma_f32 v[8:9], v[88:89], s[18:19], v[32:33] op_sel_hi:[1,0,1]
	v_pk_fma_f32 v[10:11], v[84:85], s[18:19], v[20:21] op_sel_hi:[1,0,1]
	v_lshlrev_b64 v[6:7], 11, v[6:7]
	v_cvt_pk_fp8_f32 v14, v8, v9 op_sel:[0,0,1]
	v_cvt_pk_fp8_f32 v15, v10, v11 op_sel:[0,0,1]
	v_lshl_add_u64 v[6:7], s[14:15], 0, v[6:7]
	v_lshl_add_u64 v[6:7], v[6:7], 0, v[2:3]
	global_store_dwordx2 v[6:7], v[12:13], off
	global_store_dwordx2 v[6:7], v[14:15], off offset:128
	v_pk_fma_f32 v[8:9], v[78:79], s[18:19], v[26:27] op_sel_hi:[1,0,1]
	v_pk_fma_f32 v[10:11], v[74:75], s[18:19], v[22:23] op_sel_hi:[1,0,1]
	v_cvt_pk_fp8_f32 v12, v8, v9
	v_cvt_pk_fp8_f32 v13, v10, v11
	v_pk_fma_f32 v[8:9], v[80:81], s[18:19], v[28:29] op_sel_hi:[1,0,1]
	v_pk_fma_f32 v[10:11], v[76:77], s[18:19], v[24:25] op_sel_hi:[1,0,1]
	v_cvt_pk_fp8_f32 v12, v8, v9 op_sel:[0,0,1]
	v_cvt_pk_fp8_f32 v13, v10, v11 op_sel:[0,0,1]
	v_pk_fma_f32 v[8:9], v[70:71], s[18:19], v[30:31] op_sel_hi:[1,0,1]
	v_pk_fma_f32 v[10:11], v[66:67], s[18:19], v[18:19] op_sel_hi:[1,0,1]
	v_cvt_pk_fp8_f32 v14, v8, v9
	v_cvt_pk_fp8_f32 v15, v10, v11
	v_add_u32_e32 v6, 0x90, v4
	v_ashrrev_i32_e32 v7, 31, v6
	v_pk_fma_f32 v[8:9], v[72:73], s[18:19], v[32:33] op_sel_hi:[1,0,1]
	v_pk_fma_f32 v[10:11], v[68:69], s[18:19], v[20:21] op_sel_hi:[1,0,1]
	v_lshlrev_b64 v[6:7], 11, v[6:7]
	v_cvt_pk_fp8_f32 v14, v8, v9 op_sel:[0,0,1]
	v_cvt_pk_fp8_f32 v15, v10, v11 op_sel:[0,0,1]
	v_lshl_add_u64 v[6:7], s[14:15], 0, v[6:7]
	v_lshl_add_u64 v[6:7], v[6:7], 0, v[2:3]
	global_store_dwordx2 v[6:7], v[12:13], off
	global_store_dwordx2 v[6:7], v[14:15], off offset:128
	v_pk_fma_f32 v[8:9], v[62:63], s[18:19], v[26:27] op_sel_hi:[1,0,1]
	v_pk_fma_f32 v[10:11], v[58:59], s[18:19], v[22:23] op_sel_hi:[1,0,1]
	v_cvt_pk_fp8_f32 v12, v8, v9
	v_cvt_pk_fp8_f32 v13, v10, v11
	v_pk_fma_f32 v[8:9], v[64:65], s[18:19], v[28:29] op_sel_hi:[1,0,1]
	v_pk_fma_f32 v[10:11], v[60:61], s[18:19], v[24:25] op_sel_hi:[1,0,1]
	v_cvt_pk_fp8_f32 v12, v8, v9 op_sel:[0,0,1]
	v_cvt_pk_fp8_f32 v13, v10, v11 op_sel:[0,0,1]
	v_pk_fma_f32 v[8:9], v[54:55], s[18:19], v[30:31] op_sel_hi:[1,0,1]
	v_pk_fma_f32 v[10:11], v[50:51], s[18:19], v[18:19] op_sel_hi:[1,0,1]
	v_cvt_pk_fp8_f32 v14, v8, v9
	v_cvt_pk_fp8_f32 v15, v10, v11
	v_add_u32_e32 v6, 0xa0, v4
	v_ashrrev_i32_e32 v7, 31, v6
	v_pk_fma_f32 v[8:9], v[56:57], s[18:19], v[32:33] op_sel_hi:[1,0,1]
	v_pk_fma_f32 v[10:11], v[52:53], s[18:19], v[20:21] op_sel_hi:[1,0,1]
	v_lshlrev_b64 v[6:7], 11, v[6:7]
	v_cvt_pk_fp8_f32 v14, v8, v9 op_sel:[0,0,1]
	v_cvt_pk_fp8_f32 v15, v10, v11 op_sel:[0,0,1]
	v_lshl_add_u64 v[6:7], s[14:15], 0, v[6:7]
	v_lshl_add_u64 v[6:7], v[6:7], 0, v[2:3]
	global_store_dwordx2 v[6:7], v[12:13], off
	global_store_dwordx2 v[6:7], v[14:15], off offset:128
	v_pk_fma_f32 v[6:7], v[46:47], s[18:19], v[26:27] op_sel_hi:[1,0,1]
	v_pk_fma_f32 v[8:9], v[42:43], s[18:19], v[22:23] op_sel_hi:[1,0,1]
	v_cvt_pk_fp8_f32 v10, v6, v7
	v_cvt_pk_fp8_f32 v11, v8, v9
	v_pk_fma_f32 v[6:7], v[48:49], s[18:19], v[28:29] op_sel_hi:[1,0,1]
	v_pk_fma_f32 v[8:9], v[44:45], s[18:19], v[24:25] op_sel_hi:[1,0,1]
	v_cvt_pk_fp8_f32 v10, v6, v7 op_sel:[0,0,1]
	v_cvt_pk_fp8_f32 v11, v8, v9 op_sel:[0,0,1]
	v_pk_fma_f32 v[6:7], v[38:39], s[18:19], v[30:31] op_sel_hi:[1,0,1]
	v_pk_fma_f32 v[8:9], v[34:35], s[18:19], v[18:19] op_sel_hi:[1,0,1]
	v_cvt_pk_fp8_f32 v12, v6, v7
	v_cvt_pk_fp8_f32 v13, v8, v9
	v_add_u32_e32 v4, 0xb0, v4
	v_ashrrev_i32_e32 v5, 31, v4
	v_pk_fma_f32 v[6:7], v[40:41], s[18:19], v[32:33] op_sel_hi:[1,0,1]
	v_pk_fma_f32 v[8:9], v[36:37], s[18:19], v[20:21] op_sel_hi:[1,0,1]
	v_lshlrev_b64 v[4:5], 11, v[4:5]
	v_cvt_pk_fp8_f32 v12, v6, v7 op_sel:[0,0,1]
	v_cvt_pk_fp8_f32 v13, v8, v9 op_sel:[0,0,1]
	v_lshl_add_u64 v[4:5], s[14:15], 0, v[4:5]
	v_lshl_add_u64 v[2:3], v[4:5], 0, v[2:3]
	s_andn2_b64 vcc, exec, s[0:1]
	s_mov_b64 s[0:1], -1
	global_store_dwordx2 v[2:3], v[10:11], off
	global_store_dwordx2 v[2:3], v[12:13], off offset:128
	s_cbranch_vccnz .LBB0_1001
	s_andn2_b64 vcc, exec, s[12:13]
	s_cbranch_vccnz .LBB0_1000
	s_barrier
	s_branch .LBB0_1000
